# QKV/proj/MLP2 K-loops: LDS-DMA loads use scalar base + 32-bit lane offset (saddr form), removing 15 v_lshl_add_u64 per loop body; on top of v38 stack
# speedup vs baseline: 1.0130x; 1.0054x over previous
.LBB3_32:
	v_mov_b32_e32 v47, 0
	s_andn2_b64 vcc, exec, s[18:19]
	v_mov_b32_e32 v46, v47
	v_mov_b32_e32 v45, v47
	v_mov_b32_e32 v44, v47
	v_mov_b32_e32 v43, v47
	v_mov_b32_e32 v42, v47
	v_mov_b32_e32 v41, v47
	v_mov_b32_e32 v40, v47
	v_mov_b32_e32 v39, v47
	v_mov_b32_e32 v38, v47
	v_mov_b32_e32 v37, v47
	v_mov_b32_e32 v36, v47
	v_mov_b32_e32 v35, v47
	v_mov_b32_e32 v34, v47
	v_mov_b32_e32 v33, v47
	v_mov_b32_e32 v32, v47
	v_mov_b32_e32 v31, v47
	v_mov_b32_e32 v30, v47
	v_mov_b32_e32 v29, v47
	v_mov_b32_e32 v28, v47
	v_mov_b32_e32 v27, v47
	v_mov_b32_e32 v26, v47
	v_mov_b32_e32 v25, v47
	v_mov_b32_e32 v24, v47
	v_mov_b32_e32 v23, v47
	v_mov_b32_e32 v22, v47
	v_mov_b32_e32 v21, v47
	v_mov_b32_e32 v20, v47
	v_mov_b32_e32 v19, v47
	v_mov_b32_e32 v18, v47
	v_mov_b32_e32 v17, v47
	v_mov_b32_e32 v16, v47
	v_mov_b32_e32 v15, v47
	v_mov_b32_e32 v14, v47
	v_mov_b32_e32 v13, v47
	v_mov_b32_e32 v12, v47
	v_mov_b32_e32 v11, v47
	v_mov_b32_e32 v10, v47
	v_mov_b32_e32 v9, v47
	v_mov_b32_e32 v8, v47
	v_mov_b32_e32 v7, v47
	v_mov_b32_e32 v6, v47
	v_mov_b32_e32 v5, v47
	v_mov_b32_e32 v4, v47
	v_mov_b32_e32 v3, v47
	v_mov_b32_e32 v2, v47
	v_mov_b32_e32 v1, v47
	v_mov_b32_e32 v0, v47
	s_cbranch_vccnz .LBB3_21
	v_mov_b32_e32 v0, 0
	v_lshl_add_u64 v[72:73], s[20:21], 0, v[60:61]
	v_lshl_add_u64 v[74:75], s[20:21], 0, v[62:63]
	v_lshl_add_u64 v[76:77], s[22:23], 0, v[64:65]
	v_lshl_add_u64 v[78:79], s[22:23], 0, v[66:67]
	v_lshl_add_u64 v[80:81], s[22:23], 0, v[68:69]
	s_mov_b32 s63, 0
	s_mov_b64 s[24:25], 0
	v_mov_b32_e32 v1, v0
	v_mov_b32_e32 v2, v0
	v_mov_b32_e32 v3, v0
	v_mov_b32_e32 v4, v0
	v_mov_b32_e32 v5, v0
	v_mov_b32_e32 v6, v0
	v_mov_b32_e32 v7, v0
	v_mov_b32_e32 v8, v0
	v_mov_b32_e32 v9, v0
	v_mov_b32_e32 v10, v0
	v_mov_b32_e32 v11, v0
	v_mov_b32_e32 v12, v0
	v_mov_b32_e32 v13, v0
	v_mov_b32_e32 v14, v0
	v_mov_b32_e32 v15, v0
	v_mov_b32_e32 v16, v0
	v_mov_b32_e32 v17, v0
	v_mov_b32_e32 v18, v0
	v_mov_b32_e32 v19, v0
	v_mov_b32_e32 v20, v0
	v_mov_b32_e32 v21, v0
	v_mov_b32_e32 v22, v0
	v_mov_b32_e32 v23, v0
	v_mov_b32_e32 v24, v0
	v_mov_b32_e32 v25, v0
	v_mov_b32_e32 v26, v0
	v_mov_b32_e32 v27, v0
	v_mov_b32_e32 v28, v0
	v_mov_b32_e32 v29, v0
	v_mov_b32_e32 v30, v0
	v_mov_b32_e32 v31, v0
	v_mov_b32_e32 v32, v0
	v_mov_b32_e32 v33, v0
	v_mov_b32_e32 v34, v0
	v_mov_b32_e32 v35, v0
	v_mov_b32_e32 v36, v0
	v_mov_b32_e32 v37, v0
	v_mov_b32_e32 v38, v0
	v_mov_b32_e32 v39, v0
	v_mov_b32_e32 v40, v0
	v_mov_b32_e32 v41, v0
	v_mov_b32_e32 v42, v0
	v_mov_b32_e32 v43, v0
	v_mov_b32_e32 v44, v0
	v_mov_b32_e32 v45, v0
	v_mov_b32_e32 v46, v0
	v_mov_b32_e32 v47, v0
	s_add_u32 s68, s20, s24
	s_addc_u32 s69, s21, s25
	s_add_u32 s70, s22, s24
	s_addc_u32 s71, s23, s25
	s_add_u32 s26, s20, s24
	s_addc_u32 s27, s21, s25
	s_add_u32 s26, s26, 0x180
	s_addc_u32 s27, s27, 0
	s_add_u32 s64, s22, s24
	s_addc_u32 s65, s23, s25
	s_add_u32 s66, s64, 0x180
	s_addc_u32 s67, s65, 0
	s_cmp_eq_u32 s56, s63
	s_cselect_b32 s65, s5, s27
	s_cselect_b32 s64, s4, s26
	s_cselect_b32 s27, s7, s67
	s_cselect_b32 s26, s6, s66
	s_add_u32 s72, s64, 0x80
	s_addc_u32 s73, s65, 0
	s_add_u32 s74, s26, 0x80
	s_addc_u32 s75, s27, 0
	s_add_i32 s66, s58, s38
.LBB3_34:
	s_mov_b32 m0, s66
	ds_read_b128 v[98:101], v94 offset:16384
	ds_read_b128 v[102:105], v94 offset:17408
	ds_read_b128 v[106:109], v94 offset:18432
	ds_read_b128 v[110:113], v94 offset:19456
	ds_read_b128 v[114:117], v95
	ds_read_b128 v[118:121], v95 offset:1024
	ds_read_b128 v[122:125], v95 offset:2048
	ds_read_b128 v[126:129], v95 offset:3072
	ds_read_b128 v[130:133], v95 offset:4096
	ds_read_b128 v[134:137], v95 offset:5120
	ds_read_b128 v[138:141], v95 offset:6144
	ds_read_b128 v[142:145], v95 offset:7168
	global_load_lds_dwordx4 v60, s[68:69]
	s_add_i32 m0, s66, 0x2000
	s_nop 0
	global_load_lds_dwordx4 v62, s[68:69]
	s_barrier
	s_setprio 1
	s_waitcnt lgkmcnt(7)
	v_mfma_f32_16x16x32_f16 v[44:47], v[98:101], v[114:117], v[44:47]
	v_mfma_f32_16x16x32_f16 v[40:43], v[106:109], v[114:117], v[40:43]
	s_waitcnt lgkmcnt(5)
	v_mfma_f32_16x16x32_f16 v[32:35], v[98:101], v[122:125], v[32:35]
	v_mfma_f32_16x16x32_f16 v[28:31], v[106:109], v[122:125], v[28:31]
	s_waitcnt lgkmcnt(3)
	v_mfma_f32_16x16x32_f16 v[20:23], v[98:101], v[130:133], v[20:23]
	v_mfma_f32_16x16x32_f16 v[16:19], v[106:109], v[130:133], v[16:19]
	s_waitcnt lgkmcnt(1)
	v_mfma_f32_16x16x32_f16 v[8:11], v[98:101], v[138:141], v[8:11]
	v_mfma_f32_16x16x32_f16 v[4:7], v[106:109], v[138:141], v[4:7]
	v_mfma_f32_16x16x32_f16 v[44:47], v[102:105], v[118:121], v[44:47]
	v_mfma_f32_16x16x32_f16 v[40:43], v[110:113], v[118:121], v[40:43]
	v_mfma_f32_16x16x32_f16 v[32:35], v[102:105], v[126:129], v[32:35]
	v_mfma_f32_16x16x32_f16 v[28:31], v[110:113], v[126:129], v[28:31]
	v_mfma_f32_16x16x32_f16 v[20:23], v[102:105], v[134:137], v[20:23]
	v_mfma_f32_16x16x32_f16 v[16:19], v[110:113], v[134:137], v[16:19]
	s_waitcnt lgkmcnt(0)
	v_mfma_f32_16x16x32_f16 v[8:11], v[102:105], v[142:145], v[8:11]
	v_mfma_f32_16x16x32_f16 v[4:7], v[110:113], v[142:145], v[4:7]
	s_setprio 0
	s_barrier
	s_add_i32 m0, s43, 0x18000
	ds_read_b128 v[98:101], v94 offset:20480
	ds_read_b128 v[102:105], v94 offset:21504
	global_load_lds_dwordx4 v64, s[70:71]
	s_add_i32 m0, s43, 0x1a000
	s_nop 0
	global_load_lds_dwordx4 v66, s[70:71]
	s_add_i32 m0, s43, 0x1c000
	s_nop 0
	global_load_lds_dwordx4 v68, s[70:71]
	s_waitcnt vmcnt(5)
	s_barrier
	s_setprio 1
	s_waitcnt lgkmcnt(1)
	v_mfma_f32_16x16x32_f16 v[36:39], v[98:101], v[114:117], v[36:39]
	v_mfma_f32_16x16x32_f16 v[24:27], v[98:101], v[122:125], v[24:27]
	v_mfma_f32_16x16x32_f16 v[12:15], v[98:101], v[130:133], v[12:15]
	v_mfma_f32_16x16x32_f16 v[0:3], v[98:101], v[138:141], v[0:3]
	s_waitcnt lgkmcnt(0)
	v_mfma_f32_16x16x32_f16 v[36:39], v[102:105], v[118:121], v[36:39]
	v_mfma_f32_16x16x32_f16 v[24:27], v[102:105], v[126:129], v[24:27]
	v_mfma_f32_16x16x32_f16 v[12:15], v[102:105], v[134:137], v[12:15]
	v_mfma_f32_16x16x32_f16 v[0:3], v[102:105], v[142:145], v[0:3]
	s_setprio 0
	s_barrier
	s_mov_b32 m0, s43
	ds_read_b128 v[98:101], v94 offset:57344
	ds_read_b128 v[102:105], v94 offset:58368
	ds_read_b128 v[106:109], v94 offset:59392
	ds_read_b128 v[110:113], v94 offset:60416
	ds_read_b128 v[114:117], v95 offset:40960
	ds_read_b128 v[118:121], v95 offset:41984
	ds_read_b128 v[122:125], v95 offset:43008
	ds_read_b128 v[126:129], v95 offset:44032
	ds_read_b128 v[130:133], v95 offset:45056
	ds_read_b128 v[134:137], v95 offset:46080
	ds_read_b128 v[138:141], v95 offset:47104
	ds_read_b128 v[142:145], v95 offset:48128
	global_load_lds_dwordx4 v48, s[64:65]
	s_mov_b32 m0, s44
	s_nop 0
	global_load_lds_dwordx4 v52, s[64:65]
	s_barrier
	s_setprio 1
	s_waitcnt lgkmcnt(7)
	v_mfma_f32_16x16x32_f16 v[44:47], v[98:101], v[114:117], v[44:47]
	v_mfma_f32_16x16x32_f16 v[40:43], v[106:109], v[114:117], v[40:43]
	s_waitcnt lgkmcnt(5)
	v_mfma_f32_16x16x32_f16 v[32:35], v[98:101], v[122:125], v[32:35]
	v_mfma_f32_16x16x32_f16 v[28:31], v[106:109], v[122:125], v[28:31]
	s_waitcnt lgkmcnt(3)
	v_mfma_f32_16x16x32_f16 v[20:23], v[98:101], v[130:133], v[20:23]
	v_mfma_f32_16x16x32_f16 v[16:19], v[106:109], v[130:133], v[16:19]
	s_waitcnt lgkmcnt(1)
	v_mfma_f32_16x16x32_f16 v[8:11], v[98:101], v[138:141], v[8:11]
	v_mfma_f32_16x16x32_f16 v[4:7], v[106:109], v[138:141], v[4:7]
	v_mfma_f32_16x16x32_f16 v[44:47], v[102:105], v[118:121], v[44:47]
	v_mfma_f32_16x16x32_f16 v[40:43], v[110:113], v[118:121], v[40:43]
	v_mfma_f32_16x16x32_f16 v[32:35], v[102:105], v[126:129], v[32:35]
	v_mfma_f32_16x16x32_f16 v[28:31], v[110:113], v[126:129], v[28:31]
	v_mfma_f32_16x16x32_f16 v[20:23], v[102:105], v[134:137], v[20:23]
	v_mfma_f32_16x16x32_f16 v[16:19], v[110:113], v[134:137], v[16:19]
	s_waitcnt lgkmcnt(0)
	v_mfma_f32_16x16x32_f16 v[8:11], v[102:105], v[142:145], v[8:11]
	v_mfma_f32_16x16x32_f16 v[4:7], v[110:113], v[142:145], v[4:7]
	s_setprio 0
	s_barrier
	s_mov_b32 m0, s45
	ds_read_b128 v[98:101], v94 offset:61440
	ds_read_b128 v[102:105], v94 offset:62464
	global_load_lds_dwordx4 v50, s[26:27]
	s_mov_b32 m0, s46
	s_nop 0
	global_load_lds_dwordx4 v54, s[26:27]
	s_mov_b32 m0, s47
	s_nop 0
	global_load_lds_dwordx4 v56, s[26:27]
	s_waitcnt vmcnt(5)
	s_barrier
	s_setprio 1
	s_waitcnt lgkmcnt(1)
	v_mfma_f32_16x16x32_f16 v[36:39], v[98:101], v[114:117], v[36:39]
	v_mfma_f32_16x16x32_f16 v[24:27], v[98:101], v[122:125], v[24:27]
	v_mfma_f32_16x16x32_f16 v[12:15], v[98:101], v[130:133], v[12:15]
	v_mfma_f32_16x16x32_f16 v[0:3], v[98:101], v[138:141], v[0:3]
	s_waitcnt lgkmcnt(0)
	v_mfma_f32_16x16x32_f16 v[36:39], v[102:105], v[118:121], v[36:39]
	v_mfma_f32_16x16x32_f16 v[24:27], v[102:105], v[126:129], v[24:27]
	v_mfma_f32_16x16x32_f16 v[12:15], v[102:105], v[134:137], v[12:15]
	v_mfma_f32_16x16x32_f16 v[0:3], v[102:105], v[142:145], v[0:3]
	s_setprio 0
	s_barrier
	s_mov_b32 m0, s52
	ds_read_b128 v[98:101], v96
	ds_read_b128 v[102:105], v96 offset:1024
	ds_read_b128 v[106:109], v96 offset:2048
	ds_read_b128 v[110:113], v96 offset:3072
	ds_read_b128 v[114:117], v97
	ds_read_b128 v[118:121], v97 offset:1024
	ds_read_b128 v[122:125], v97 offset:2048
	ds_read_b128 v[126:129], v97 offset:3072
	ds_read_b128 v[130:133], v97 offset:4096
	ds_read_b128 v[134:137], v97 offset:5120
	ds_read_b128 v[138:141], v97 offset:6144
	ds_read_b128 v[142:145], v97 offset:7168
	global_load_lds_dwordx4 v48, s[72:73]
	s_mov_b32 m0, s53
	s_nop 0
	global_load_lds_dwordx4 v52, s[72:73]
	s_barrier
	s_setprio 1
	s_waitcnt lgkmcnt(7)
	v_mfma_f32_16x16x32_f16 v[44:47], v[98:101], v[114:117], v[44:47]
	v_mfma_f32_16x16x32_f16 v[40:43], v[106:109], v[114:117], v[40:43]
	s_waitcnt lgkmcnt(5)
	v_mfma_f32_16x16x32_f16 v[32:35], v[98:101], v[122:125], v[32:35]
	v_mfma_f32_16x16x32_f16 v[28:31], v[106:109], v[122:125], v[28:31]
	s_waitcnt lgkmcnt(3)
	v_mfma_f32_16x16x32_f16 v[20:23], v[98:101], v[130:133], v[20:23]
	v_mfma_f32_16x16x32_f16 v[16:19], v[106:109], v[130:133], v[16:19]
	s_waitcnt lgkmcnt(1)
	v_mfma_f32_16x16x32_f16 v[8:11], v[98:101], v[138:141], v[8:11]
	v_mfma_f32_16x16x32_f16 v[4:7], v[106:109], v[138:141], v[4:7]
	v_mfma_f32_16x16x32_f16 v[44:47], v[102:105], v[118:121], v[44:47]
	v_mfma_f32_16x16x32_f16 v[40:43], v[110:113], v[118:121], v[40:43]
	v_mfma_f32_16x16x32_f16 v[32:35], v[102:105], v[126:129], v[32:35]
	v_mfma_f32_16x16x32_f16 v[28:31], v[110:113], v[126:129], v[28:31]
	v_mfma_f32_16x16x32_f16 v[20:23], v[102:105], v[134:137], v[20:23]
	v_mfma_f32_16x16x32_f16 v[16:19], v[110:113], v[134:137], v[16:19]
	s_waitcnt lgkmcnt(0)
	v_mfma_f32_16x16x32_f16 v[8:11], v[102:105], v[142:145], v[8:11]
	v_mfma_f32_16x16x32_f16 v[4:7], v[110:113], v[142:145], v[4:7]
	s_setprio 0
	s_barrier
	s_mov_b32 m0, s54
	ds_read_b128 v[98:101], v96 offset:4096
	ds_read_b128 v[102:105], v96 offset:5120
	global_load_lds_dwordx4 v50, s[74:75]
	s_add_i32 m0, s54, 0x2000
	s_nop 0
	global_load_lds_dwordx4 v54, s[74:75]
	s_add_i32 m0, s54, 0x4000
	s_nop 0
	global_load_lds_dwordx4 v56, s[74:75]
	s_waitcnt vmcnt(5)
	s_barrier
	s_setprio 1
	s_waitcnt lgkmcnt(1)
	v_mfma_f32_16x16x32_f16 v[36:39], v[98:101], v[114:117], v[36:39]
	v_mfma_f32_16x16x32_f16 v[24:27], v[98:101], v[122:125], v[24:27]
	v_mfma_f32_16x16x32_f16 v[12:15], v[98:101], v[130:133], v[12:15]
	v_mfma_f32_16x16x32_f16 v[0:3], v[98:101], v[138:141], v[0:3]
	s_waitcnt lgkmcnt(0)
	v_mfma_f32_16x16x32_f16 v[36:39], v[102:105], v[118:121], v[36:39]
	v_mfma_f32_16x16x32_f16 v[24:27], v[102:105], v[126:129], v[24:27]
	v_mfma_f32_16x16x32_f16 v[12:15], v[102:105], v[134:137], v[12:15]
	v_mfma_f32_16x16x32_f16 v[0:3], v[102:105], v[142:145], v[0:3]
	s_setprio 0
	s_add_i32 s63, s63, 3
	s_add_u32 s24, s24, 0x180
	s_addc_u32 s25, s25, 0
	s_cmp_ge_i32 s63, s49
	s_cbranch_scc1 .Lrot_exit_qkv
	s_add_u32 s68, s20, s24
	s_addc_u32 s69, s21, s25
	s_add_u32 s70, s22, s24
	s_addc_u32 s71, s23, s25
	s_add_u32 s26, s20, s24
	s_addc_u32 s27, s21, s25
	s_add_u32 s26, s26, 0x180
	s_addc_u32 s27, s27, 0
	s_add_u32 s64, s22, s24
	s_addc_u32 s65, s23, s25
	s_add_u32 s66, s64, 0x180
	s_addc_u32 s67, s65, 0
	s_cmp_eq_u32 s56, s63
	s_cselect_b32 s65, s5, s27
	s_cselect_b32 s64, s4, s26
	s_cselect_b32 s27, s7, s67
	s_cselect_b32 s26, s6, s66
	s_add_u32 s72, s64, 0x80
	s_addc_u32 s73, s65, 0
	s_add_u32 s74, s26, 0x80
	s_addc_u32 s75, s27, 0
	s_add_i32 s66, s58, s38
	s_barrier
	s_branch .LBB3_34

	.amdhsa_kernel _Z9k_gemm192IN4g1926EpiQKVEEvNS0_4GemmET_
		.amdhsa_group_segment_fixed_size 0
		.amdhsa_private_segment_fixed_size 0
		.amdhsa_kernarg_size 328
		.amdhsa_user_sgpr_count 2
		.amdhsa_user_sgpr_dispatch_ptr 0
		.amdhsa_user_sgpr_queue_ptr 0
		.amdhsa_user_sgpr_kernarg_segment_ptr 1
		.amdhsa_user_sgpr_dispatch_id 0
		.amdhsa_user_sgpr_kernarg_preload_length 0
		.amdhsa_user_sgpr_kernarg_preload_offset 0
		.amdhsa_user_sgpr_private_segment_size 0
		.amdhsa_uses_dynamic_stack 0
		.amdhsa_enable_private_segment 0
		.amdhsa_system_sgpr_workgroup_id_x 1
		.amdhsa_system_sgpr_workgroup_id_y 0
		.amdhsa_system_sgpr_workgroup_id_z 0
		.amdhsa_system_sgpr_workgroup_info 0
		.amdhsa_system_vgpr_workitem_id 0
		.amdhsa_next_free_vgpr 156
		.amdhsa_next_free_sgpr 76
		.amdhsa_accum_offset 156
		.amdhsa_reserve_vcc 1
		.amdhsa_float_round_mode_32 0
		.amdhsa_float_round_mode_16_64 0
		.amdhsa_float_denorm_mode_32 3
		.amdhsa_float_denorm_mode_16_64 3
		.amdhsa_dx10_clamp 1
		.amdhsa_ieee_mode 1
		.amdhsa_fp16_overflow 0
		.amdhsa_tg_split 0
		.amdhsa_exception_fp_ieee_invalid_op 0
		.amdhsa_exception_fp_denorm_src 0
		.amdhsa_exception_fp_ieee_div_zero 0
		.amdhsa_exception_fp_ieee_overflow 0
		.amdhsa_exception_fp_ieee_underflow 0
		.amdhsa_exception_fp_ieee_inexact 0
		.amdhsa_exception_int_div_zero 0
	.end_amdhsa_kernel

.LBB4_20:
	v_mov_b32_e32 v97, 0
	s_andn2_b64 vcc, exec, s[24:25]
	v_mov_b32_e32 v96, v97
	v_mov_b32_e32 v95, v97
	v_mov_b32_e32 v94, v97
	v_mov_b32_e32 v93, v97
	v_mov_b32_e32 v92, v97
	v_mov_b32_e32 v91, v97
	v_mov_b32_e32 v90, v97
	v_mov_b32_e32 v89, v97
	v_mov_b32_e32 v88, v97
	v_mov_b32_e32 v87, v97
	v_mov_b32_e32 v86, v97
	v_mov_b32_e32 v85, v97
	v_mov_b32_e32 v84, v97
	v_mov_b32_e32 v83, v97
	v_mov_b32_e32 v82, v97
	v_mov_b32_e32 v81, v97
	v_mov_b32_e32 v80, v97
	v_mov_b32_e32 v79, v97
	v_mov_b32_e32 v78, v97
	v_mov_b32_e32 v77, v97
	v_mov_b32_e32 v76, v97
	v_mov_b32_e32 v75, v97
	v_mov_b32_e32 v74, v97
	v_mov_b32_e32 v73, v97
	v_mov_b32_e32 v72, v97
	v_mov_b32_e32 v71, v97
	v_mov_b32_e32 v70, v97
	v_mov_b32_e32 v69, v97
	v_mov_b32_e32 v68, v97
	v_mov_b32_e32 v67, v97
	v_mov_b32_e32 v66, v97
	v_mov_b32_e32 v65, v97
	v_mov_b32_e32 v64, v97
	v_mov_b32_e32 v63, v97
	v_mov_b32_e32 v62, v97
	v_mov_b32_e32 v61, v97
	v_mov_b32_e32 v60, v97
	v_mov_b32_e32 v59, v97
	v_mov_b32_e32 v58, v97
	v_mov_b32_e32 v57, v97
	v_mov_b32_e32 v56, v97
	v_mov_b32_e32 v55, v97
	v_mov_b32_e32 v54, v97
	s_waitcnt lgkmcnt(0)
	v_mov_b32_e32 v53, v97
	v_mov_b32_e32 v52, v97
	v_mov_b32_e32 v51, v97
	v_mov_b32_e32 v50, v97
	s_cbranch_vccnz .LBB4_23
	v_mov_b32_e32 v50, 0
	v_lshl_add_u64 v[98:99], s[26:27], 0, v[0:1]
	v_lshl_add_u64 v[100:101], s[26:27], 0, v[120:121]
	v_lshl_add_u64 v[102:103], s[28:29], 0, v[122:123]
	v_lshl_add_u64 v[104:105], s[28:29], 0, v[124:125]
	v_lshl_add_u64 v[106:107], s[28:29], 0, v[126:127]
	s_mov_b32 s67, 0
	s_mov_b64 s[30:31], 0
	v_mov_b32_e32 v51, v50
	v_mov_b32_e32 v52, v50
	v_mov_b32_e32 v53, v50
	v_mov_b32_e32 v54, v50
	v_mov_b32_e32 v55, v50
	v_mov_b32_e32 v56, v50
	v_mov_b32_e32 v57, v50
	v_mov_b32_e32 v58, v50
	v_mov_b32_e32 v59, v50
	v_mov_b32_e32 v60, v50
	v_mov_b32_e32 v61, v50
	v_mov_b32_e32 v62, v50
	v_mov_b32_e32 v63, v50
	v_mov_b32_e32 v64, v50
	v_mov_b32_e32 v65, v50
	v_mov_b32_e32 v66, v50
	v_mov_b32_e32 v67, v50
	v_mov_b32_e32 v68, v50
	v_mov_b32_e32 v69, v50
	v_mov_b32_e32 v70, v50
	v_mov_b32_e32 v71, v50
	v_mov_b32_e32 v72, v50
	v_mov_b32_e32 v73, v50
	v_mov_b32_e32 v74, v50
	v_mov_b32_e32 v75, v50
	v_mov_b32_e32 v76, v50
	v_mov_b32_e32 v77, v50
	v_mov_b32_e32 v78, v50
	v_mov_b32_e32 v79, v50
	v_mov_b32_e32 v80, v50
	v_mov_b32_e32 v81, v50
	v_mov_b32_e32 v82, v50
	v_mov_b32_e32 v83, v50
	v_mov_b32_e32 v84, v50
	v_mov_b32_e32 v85, v50
	v_mov_b32_e32 v86, v50
	v_mov_b32_e32 v87, v50
	v_mov_b32_e32 v88, v50
	v_mov_b32_e32 v89, v50
	v_mov_b32_e32 v90, v50
	v_mov_b32_e32 v91, v50
	v_mov_b32_e32 v92, v50
	v_mov_b32_e32 v93, v50
	v_mov_b32_e32 v94, v50
	v_mov_b32_e32 v95, v50
	v_mov_b32_e32 v96, v50
	v_mov_b32_e32 v97, v50
	s_add_u32 s74, s26, s30
	s_addc_u32 s75, s27, s31
	s_add_u32 s76, s28, s30
	s_addc_u32 s77, s29, s31
	s_add_u32 s34, s26, s30
	s_addc_u32 s35, s27, s31
	s_add_u32 s34, s34, 0x180
	s_addc_u32 s35, s35, 0
	s_add_u32 s68, s28, s30
	s_addc_u32 s69, s29, s31
	s_add_u32 s70, s68, 0x180
	s_addc_u32 s71, s69, 0
	s_cmp_eq_u32 s60, s67
	s_cselect_b32 s69, s5, s35
	s_cselect_b32 s68, s4, s34
	s_cselect_b32 s35, s7, s71
	s_cselect_b32 s34, s6, s70
	s_add_u32 s78, s68, 0x80
	s_addc_u32 s79, s69, 0
	s_add_u32 s80, s34, 0x80
	s_addc_u32 s81, s35, 0
	s_add_i32 s70, s62, s44
.LBB4_22:
	s_mov_b32 m0, s70
	ds_read_b128 v[130:133], v136 offset:16384
	ds_read_b128 v[142:145], v136 offset:17408
	ds_read_b128 v[146:149], v136 offset:18432
	ds_read_b128 v[150:153], v136 offset:19456
	ds_read_b128 v[154:157], v137
	ds_read_b128 v[158:161], v137 offset:1024
	ds_read_b128 v[162:165], v137 offset:2048
	ds_read_b128 v[166:169], v137 offset:3072
	ds_read_b128 v[170:173], v137 offset:4096
	ds_read_b128 v[174:177], v137 offset:5120
	ds_read_b128 v[178:181], v137 offset:6144
	ds_read_b128 v[182:185], v137 offset:7168
	global_load_lds_dwordx4 v0, s[74:75]
	s_add_i32 m0, s70, 0x2000
	s_nop 0
	global_load_lds_dwordx4 v120, s[74:75]
	s_barrier
	s_setprio 1
	s_waitcnt lgkmcnt(7)
	v_mfma_f32_16x16x32_f16 v[94:97], v[130:133], v[154:157], v[94:97]
	v_mfma_f32_16x16x32_f16 v[90:93], v[146:149], v[154:157], v[90:93]
	s_waitcnt lgkmcnt(5)
	v_mfma_f32_16x16x32_f16 v[82:85], v[130:133], v[162:165], v[82:85]
	v_mfma_f32_16x16x32_f16 v[78:81], v[146:149], v[162:165], v[78:81]
	s_waitcnt lgkmcnt(3)
	v_mfma_f32_16x16x32_f16 v[70:73], v[130:133], v[170:173], v[70:73]
	v_mfma_f32_16x16x32_f16 v[66:69], v[146:149], v[170:173], v[66:69]
	s_waitcnt lgkmcnt(1)
	v_mfma_f32_16x16x32_f16 v[58:61], v[130:133], v[178:181], v[58:61]
	v_mfma_f32_16x16x32_f16 v[54:57], v[146:149], v[178:181], v[54:57]
	v_mfma_f32_16x16x32_f16 v[94:97], v[142:145], v[158:161], v[94:97]
	v_mfma_f32_16x16x32_f16 v[90:93], v[150:153], v[158:161], v[90:93]
	v_mfma_f32_16x16x32_f16 v[82:85], v[142:145], v[166:169], v[82:85]
	v_mfma_f32_16x16x32_f16 v[78:81], v[150:153], v[166:169], v[78:81]
	v_mfma_f32_16x16x32_f16 v[70:73], v[142:145], v[174:177], v[70:73]
	v_mfma_f32_16x16x32_f16 v[66:69], v[150:153], v[174:177], v[66:69]
	s_waitcnt lgkmcnt(0)
	v_mfma_f32_16x16x32_f16 v[58:61], v[142:145], v[182:185], v[58:61]
	v_mfma_f32_16x16x32_f16 v[54:57], v[150:153], v[182:185], v[54:57]
	s_setprio 0
	s_barrier
	s_add_i32 m0, s49, 0x18000
	ds_read_b128 v[130:133], v136 offset:20480
	ds_read_b128 v[142:145], v136 offset:21504
	global_load_lds_dwordx4 v122, s[76:77]
	s_add_i32 m0, s49, 0x1a000
	s_nop 0
	global_load_lds_dwordx4 v124, s[76:77]
	s_add_i32 m0, s49, 0x1c000
	s_nop 0
	global_load_lds_dwordx4 v126, s[76:77]
	s_cmp_lg_u32 s67, 0
	s_cbranch_scc1 .Lpj_norm_0
	s_mul_i32 s72, s66, 0xc0
	v_add_u32_e32 v214, s72, v135
	v_ashrrev_i32_e32 v215, 31, v214
	v_lshl_add_u64 v[214:215], v[214:215], 2, s[10:11]
	global_load_dwordx4 v[202:205], v[214:215], off
	global_load_dwordx4 v[206:209], v[214:215], off offset:64
	global_load_dwordx4 v[210:213], v[214:215], off offset:128
	global_load_dwordx4 v[2:5], v[194:195], off
	global_load_dwordx4 v[6:9], v[194:195], off offset:64
	global_load_dwordx4 v[10:13], v[194:195], off offset:128
	global_load_dwordx4 v[14:17], v[196:197], off
	s_waitcnt vmcnt(12)
	s_branch .Lpj_join_0

.Lpj_join_0:
	s_barrier
	s_setprio 1
	s_waitcnt lgkmcnt(1)
	v_mfma_f32_16x16x32_f16 v[86:89], v[130:133], v[154:157], v[86:89]
	v_mfma_f32_16x16x32_f16 v[74:77], v[130:133], v[162:165], v[74:77]
	v_mfma_f32_16x16x32_f16 v[62:65], v[130:133], v[170:173], v[62:65]
	v_mfma_f32_16x16x32_f16 v[50:53], v[130:133], v[178:181], v[50:53]
	s_waitcnt lgkmcnt(0)
	v_mfma_f32_16x16x32_f16 v[86:89], v[142:145], v[158:161], v[86:89]
	v_mfma_f32_16x16x32_f16 v[74:77], v[142:145], v[166:169], v[74:77]
	v_mfma_f32_16x16x32_f16 v[62:65], v[142:145], v[174:177], v[62:65]
	v_mfma_f32_16x16x32_f16 v[50:53], v[142:145], v[182:185], v[50:53]
	s_setprio 0
	s_barrier
	s_mov_b32 m0, s49
	ds_read_b128 v[130:133], v136 offset:57344
	ds_read_b128 v[142:145], v136 offset:58368
	ds_read_b128 v[146:149], v136 offset:59392
	ds_read_b128 v[150:153], v136 offset:60416
	ds_read_b128 v[154:157], v137 offset:40960
	ds_read_b128 v[158:161], v137 offset:41984
	ds_read_b128 v[162:165], v137 offset:43008
	ds_read_b128 v[166:169], v137 offset:44032
	ds_read_b128 v[170:173], v137 offset:45056
	ds_read_b128 v[174:177], v137 offset:46080
	ds_read_b128 v[178:181], v137 offset:47104
	ds_read_b128 v[182:185], v137 offset:48128
	global_load_lds_dwordx4 v110, s[68:69]
	s_mov_b32 m0, s50
	s_nop 0
	global_load_lds_dwordx4 v114, s[68:69]
	s_barrier
	s_setprio 1
	s_waitcnt lgkmcnt(7)
	v_mfma_f32_16x16x32_f16 v[94:97], v[130:133], v[154:157], v[94:97]
	v_mfma_f32_16x16x32_f16 v[90:93], v[146:149], v[154:157], v[90:93]
	s_waitcnt lgkmcnt(5)
	v_mfma_f32_16x16x32_f16 v[82:85], v[130:133], v[162:165], v[82:85]
	v_mfma_f32_16x16x32_f16 v[78:81], v[146:149], v[162:165], v[78:81]
	s_waitcnt lgkmcnt(3)
	v_mfma_f32_16x16x32_f16 v[70:73], v[130:133], v[170:173], v[70:73]
	v_mfma_f32_16x16x32_f16 v[66:69], v[146:149], v[170:173], v[66:69]
	s_waitcnt lgkmcnt(1)
	v_mfma_f32_16x16x32_f16 v[58:61], v[130:133], v[178:181], v[58:61]
	v_mfma_f32_16x16x32_f16 v[54:57], v[146:149], v[178:181], v[54:57]
	v_mfma_f32_16x16x32_f16 v[94:97], v[142:145], v[158:161], v[94:97]
	v_mfma_f32_16x16x32_f16 v[90:93], v[150:153], v[158:161], v[90:93]
	v_mfma_f32_16x16x32_f16 v[82:85], v[142:145], v[166:169], v[82:85]
	v_mfma_f32_16x16x32_f16 v[78:81], v[150:153], v[166:169], v[78:81]
	v_mfma_f32_16x16x32_f16 v[70:73], v[142:145], v[174:177], v[70:73]
	v_mfma_f32_16x16x32_f16 v[66:69], v[150:153], v[174:177], v[66:69]
	s_waitcnt lgkmcnt(0)
	v_mfma_f32_16x16x32_f16 v[58:61], v[142:145], v[182:185], v[58:61]
	v_mfma_f32_16x16x32_f16 v[54:57], v[150:153], v[182:185], v[54:57]
	s_setprio 0
	s_barrier
	s_mov_b32 m0, s51
	ds_read_b128 v[130:133], v136 offset:61440
	ds_read_b128 v[142:145], v136 offset:62464
	global_load_lds_dwordx4 v112, s[34:35]
	s_mov_b32 m0, s52
	s_nop 0
	global_load_lds_dwordx4 v116, s[34:35]
	s_mov_b32 m0, s53
	s_nop 0
	global_load_lds_dwordx4 v118, s[34:35]
	s_cmp_lg_u32 s67, 0
	s_cbranch_scc1 .Lpj_norm_1
	global_load_dwordx4 v[18:21], v[196:197], off offset:64
	global_load_dwordx4 v[22:25], v[196:197], off offset:128
	global_load_dwordx4 v[26:29], v[198:199], off
	global_load_dwordx4 v[30:33], v[198:199], off offset:64
	s_waitcnt vmcnt(16)
	s_branch .Lpj_join_1

.Lpj_join_1:
	s_barrier
	s_setprio 1
	s_waitcnt lgkmcnt(1)
	v_mfma_f32_16x16x32_f16 v[86:89], v[130:133], v[154:157], v[86:89]
	v_mfma_f32_16x16x32_f16 v[74:77], v[130:133], v[162:165], v[74:77]
	v_mfma_f32_16x16x32_f16 v[62:65], v[130:133], v[170:173], v[62:65]
	v_mfma_f32_16x16x32_f16 v[50:53], v[130:133], v[178:181], v[50:53]
	s_waitcnt lgkmcnt(0)
	v_mfma_f32_16x16x32_f16 v[86:89], v[142:145], v[158:161], v[86:89]
	v_mfma_f32_16x16x32_f16 v[74:77], v[142:145], v[166:169], v[74:77]
	v_mfma_f32_16x16x32_f16 v[62:65], v[142:145], v[174:177], v[62:65]
	v_mfma_f32_16x16x32_f16 v[50:53], v[142:145], v[182:185], v[50:53]
	s_setprio 0
	s_barrier
	s_mov_b32 m0, s56
	ds_read_b128 v[130:133], v138
	ds_read_b128 v[142:145], v138 offset:1024
	ds_read_b128 v[146:149], v138 offset:2048
	ds_read_b128 v[150:153], v138 offset:3072
	ds_read_b128 v[154:157], v139
	ds_read_b128 v[158:161], v139 offset:1024
	ds_read_b128 v[162:165], v139 offset:2048
	ds_read_b128 v[166:169], v139 offset:3072
	ds_read_b128 v[170:173], v139 offset:4096
	ds_read_b128 v[174:177], v139 offset:5120
	ds_read_b128 v[178:181], v139 offset:6144
	ds_read_b128 v[182:185], v139 offset:7168
	global_load_lds_dwordx4 v110, s[78:79]
	s_mov_b32 m0, s57
	s_nop 0
	global_load_lds_dwordx4 v114, s[78:79]
	s_barrier
	s_setprio 1
	s_waitcnt lgkmcnt(7)
	v_mfma_f32_16x16x32_f16 v[94:97], v[130:133], v[154:157], v[94:97]
	v_mfma_f32_16x16x32_f16 v[90:93], v[146:149], v[154:157], v[90:93]
	s_waitcnt lgkmcnt(5)
	v_mfma_f32_16x16x32_f16 v[82:85], v[130:133], v[162:165], v[82:85]
	v_mfma_f32_16x16x32_f16 v[78:81], v[146:149], v[162:165], v[78:81]
	s_waitcnt lgkmcnt(3)
	v_mfma_f32_16x16x32_f16 v[70:73], v[130:133], v[170:173], v[70:73]
	v_mfma_f32_16x16x32_f16 v[66:69], v[146:149], v[170:173], v[66:69]
	s_waitcnt lgkmcnt(1)
	v_mfma_f32_16x16x32_f16 v[58:61], v[130:133], v[178:181], v[58:61]
	v_mfma_f32_16x16x32_f16 v[54:57], v[146:149], v[178:181], v[54:57]
	v_mfma_f32_16x16x32_f16 v[94:97], v[142:145], v[158:161], v[94:97]
	v_mfma_f32_16x16x32_f16 v[90:93], v[150:153], v[158:161], v[90:93]
	v_mfma_f32_16x16x32_f16 v[82:85], v[142:145], v[166:169], v[82:85]
	v_mfma_f32_16x16x32_f16 v[78:81], v[150:153], v[166:169], v[78:81]
	v_mfma_f32_16x16x32_f16 v[70:73], v[142:145], v[174:177], v[70:73]
	v_mfma_f32_16x16x32_f16 v[66:69], v[150:153], v[174:177], v[66:69]
	s_waitcnt lgkmcnt(0)
	v_mfma_f32_16x16x32_f16 v[58:61], v[142:145], v[182:185], v[58:61]
	v_mfma_f32_16x16x32_f16 v[54:57], v[150:153], v[182:185], v[54:57]
	s_setprio 0
	s_barrier
	s_mov_b32 m0, s58
	ds_read_b128 v[130:133], v138 offset:4096
	ds_read_b128 v[142:145], v138 offset:5120
	global_load_lds_dwordx4 v112, s[80:81]
	s_add_i32 m0, s58, 0x2000
	s_nop 0
	global_load_lds_dwordx4 v116, s[80:81]
	s_add_i32 m0, s58, 0x4000
	s_nop 0
	global_load_lds_dwordx4 v118, s[80:81]
	s_cmp_lg_u32 s67, 0
	s_cbranch_scc1 .Lpj_norm_2
	global_load_dwordx4 v[34:37], v[198:199], off offset:128
	global_load_dwordx4 v[38:41], v[200:201], off
	global_load_dwordx4 v[42:45], v[200:201], off offset:64
	global_load_dwordx4 v[46:49], v[200:201], off offset:128
	s_waitcnt vmcnt(13)
	s_branch .Lpj_join_2

.Lpj_join_2:
	s_barrier
	s_setprio 1
	s_waitcnt lgkmcnt(1)
	v_mfma_f32_16x16x32_f16 v[86:89], v[130:133], v[154:157], v[86:89]
	v_mfma_f32_16x16x32_f16 v[74:77], v[130:133], v[162:165], v[74:77]
	v_mfma_f32_16x16x32_f16 v[62:65], v[130:133], v[170:173], v[62:65]
	v_mfma_f32_16x16x32_f16 v[50:53], v[130:133], v[178:181], v[50:53]
	s_waitcnt lgkmcnt(0)
	v_mfma_f32_16x16x32_f16 v[86:89], v[142:145], v[158:161], v[86:89]
	v_mfma_f32_16x16x32_f16 v[74:77], v[142:145], v[166:169], v[74:77]
	v_mfma_f32_16x16x32_f16 v[62:65], v[142:145], v[174:177], v[62:65]
	v_mfma_f32_16x16x32_f16 v[50:53], v[142:145], v[182:185], v[50:53]
	s_setprio 0
	s_add_i32 s67, s67, 3
	s_add_u32 s30, s30, 0x180
	s_addc_u32 s31, s31, 0
	s_cmp_ge_i32 s67, s59
	s_cbranch_scc1 .Lrot_exit_proj
	s_add_u32 s74, s26, s30
	s_addc_u32 s75, s27, s31
	s_add_u32 s76, s28, s30
	s_addc_u32 s77, s29, s31
	s_add_u32 s34, s26, s30
	s_addc_u32 s35, s27, s31
	s_add_u32 s34, s34, 0x180
	s_addc_u32 s35, s35, 0
	s_add_u32 s68, s28, s30
	s_addc_u32 s69, s29, s31
	s_add_u32 s70, s68, 0x180
	s_addc_u32 s71, s69, 0
	s_cmp_eq_u32 s60, s67
	s_cselect_b32 s69, s5, s35
	s_cselect_b32 s68, s4, s34
	s_cselect_b32 s35, s7, s71
	s_cselect_b32 s34, s6, s70
	s_add_u32 s78, s68, 0x80
	s_addc_u32 s79, s69, 0
	s_add_u32 s80, s34, 0x80
	s_addc_u32 s81, s35, 0
	s_add_i32 s70, s62, s44
	s_barrier
	s_branch .LBB4_22

	.amdhsa_kernel _Z9k_gemm192IN4g19210EpiResStatEEvNS0_4GemmET_
		.amdhsa_group_segment_fixed_size 0
		.amdhsa_private_segment_fixed_size 0
		.amdhsa_kernarg_size 344
		.amdhsa_user_sgpr_count 2
		.amdhsa_user_sgpr_dispatch_ptr 0
		.amdhsa_user_sgpr_queue_ptr 0
		.amdhsa_user_sgpr_kernarg_segment_ptr 1
		.amdhsa_user_sgpr_dispatch_id 0
		.amdhsa_user_sgpr_kernarg_preload_length 0
		.amdhsa_user_sgpr_kernarg_preload_offset 0
		.amdhsa_user_sgpr_private_segment_size 0
		.amdhsa_uses_dynamic_stack 0
		.amdhsa_enable_private_segment 0
		.amdhsa_system_sgpr_workgroup_id_x 1
		.amdhsa_system_sgpr_workgroup_id_y 0
		.amdhsa_system_sgpr_workgroup_id_z 0
		.amdhsa_system_sgpr_workgroup_info 0
		.amdhsa_system_vgpr_workitem_id 0
		.amdhsa_next_free_vgpr 216
		.amdhsa_next_free_sgpr 82
		.amdhsa_accum_offset 216
		.amdhsa_reserve_vcc 1
		.amdhsa_float_round_mode_32 0
		.amdhsa_float_round_mode_16_64 0
		.amdhsa_float_denorm_mode_32 3
		.amdhsa_float_denorm_mode_16_64 3
		.amdhsa_dx10_clamp 1
		.amdhsa_ieee_mode 1
		.amdhsa_fp16_overflow 0
		.amdhsa_tg_split 0
		.amdhsa_exception_fp_ieee_invalid_op 0
		.amdhsa_exception_fp_denorm_src 0
		.amdhsa_exception_fp_ieee_div_zero 0
		.amdhsa_exception_fp_ieee_overflow 0
		.amdhsa_exception_fp_ieee_underflow 0
		.amdhsa_exception_fp_ieee_inexact 0
		.amdhsa_exception_int_div_zero 0
	.end_amdhsa_kernel

.LBB6_20:
	v_mov_b32_e32 v43, 0
	s_andn2_b64 vcc, exec, s[6:7]
	v_mov_b32_e32 v42, v43
	v_mov_b32_e32 v41, v43
	v_mov_b32_e32 v40, v43
	v_mov_b32_e32 v47, v43
	v_mov_b32_e32 v46, v43
	v_mov_b32_e32 v45, v43
	v_mov_b32_e32 v44, v43
	v_mov_b32_e32 v39, v43
	v_mov_b32_e32 v38, v43
	v_mov_b32_e32 v37, v43
	v_mov_b32_e32 v36, v43
	v_mov_b32_e32 v35, v43
	v_mov_b32_e32 v34, v43
	v_mov_b32_e32 v33, v43
	v_mov_b32_e32 v32, v43
	v_mov_b32_e32 v31, v43
	v_mov_b32_e32 v30, v43
	v_mov_b32_e32 v29, v43
	v_mov_b32_e32 v28, v43
	v_mov_b32_e32 v27, v43
	v_mov_b32_e32 v26, v43
	v_mov_b32_e32 v25, v43
	v_mov_b32_e32 v24, v43
	v_mov_b32_e32 v23, v43
	v_mov_b32_e32 v22, v43
	v_mov_b32_e32 v21, v43
	v_mov_b32_e32 v20, v43
	v_mov_b32_e32 v19, v43
	v_mov_b32_e32 v18, v43
	v_mov_b32_e32 v17, v43
	v_mov_b32_e32 v16, v43
	v_mov_b32_e32 v15, v43
	v_mov_b32_e32 v14, v43
	v_mov_b32_e32 v13, v43
	v_mov_b32_e32 v12, v43
	v_mov_b32_e32 v11, v43
	v_mov_b32_e32 v10, v43
	v_mov_b32_e32 v9, v43
	v_mov_b32_e32 v8, v43
	v_mov_b32_e32 v7, v43
	v_mov_b32_e32 v6, v43
	v_mov_b32_e32 v5, v43
	v_mov_b32_e32 v4, v43
	v_mov_b32_e32 v3, v43
	v_mov_b32_e32 v2, v43
	v_mov_b32_e32 v1, v43
	v_mov_b32_e32 v0, v43
	s_cbranch_vccnz .LBB6_9
	v_mov_b32_e32 v0, 0
	v_lshl_add_u64 v[116:117], s[22:23], 0, v[106:107]
	v_lshl_add_u64 v[118:119], s[22:23], 0, v[108:109]
	v_lshl_add_u64 v[120:121], s[24:25], 0, v[110:111]
	v_lshl_add_u64 v[122:123], s[24:25], 0, v[112:113]
	v_lshl_add_u64 v[124:125], s[24:25], 0, v[114:115]
	s_mov_b32 s65, 0
	s_mov_b64 s[28:29], 0
	v_mov_b32_e32 v1, v0
	v_mov_b32_e32 v2, v0
	v_mov_b32_e32 v3, v0
	v_mov_b32_e32 v4, v0
	v_mov_b32_e32 v5, v0
	v_mov_b32_e32 v6, v0
	v_mov_b32_e32 v7, v0
	v_mov_b32_e32 v8, v0
	v_mov_b32_e32 v9, v0
	v_mov_b32_e32 v10, v0
	v_mov_b32_e32 v11, v0
	v_mov_b32_e32 v12, v0
	v_mov_b32_e32 v13, v0
	v_mov_b32_e32 v14, v0
	v_mov_b32_e32 v15, v0
	v_mov_b32_e32 v16, v0
	v_mov_b32_e32 v17, v0
	v_mov_b32_e32 v18, v0
	v_mov_b32_e32 v19, v0
	v_mov_b32_e32 v20, v0
	v_mov_b32_e32 v21, v0
	v_mov_b32_e32 v22, v0
	v_mov_b32_e32 v23, v0
	v_mov_b32_e32 v24, v0
	v_mov_b32_e32 v25, v0
	v_mov_b32_e32 v26, v0
	v_mov_b32_e32 v27, v0
	v_mov_b32_e32 v28, v0
	v_mov_b32_e32 v29, v0
	v_mov_b32_e32 v30, v0
	v_mov_b32_e32 v31, v0
	v_mov_b32_e32 v32, v0
	v_mov_b32_e32 v33, v0
	v_mov_b32_e32 v34, v0
	v_mov_b32_e32 v35, v0
	v_mov_b32_e32 v36, v0
	v_mov_b32_e32 v37, v0
	v_mov_b32_e32 v38, v0
	v_mov_b32_e32 v39, v0
	v_mov_b32_e32 v44, v0
	v_mov_b32_e32 v45, v0
	v_mov_b32_e32 v46, v0
	v_mov_b32_e32 v47, v0
	v_mov_b32_e32 v40, v0
	v_mov_b32_e32 v41, v0
	v_mov_b32_e32 v42, v0
	v_mov_b32_e32 v43, v0
	s_add_u32 s72, s22, s28
	s_addc_u32 s73, s23, s29
	s_add_u32 s74, s24, s28
	s_addc_u32 s75, s25, s29
	s_add_u32 s30, s22, s28
	s_addc_u32 s31, s23, s29
	s_add_u32 s30, s30, 0x180
	s_addc_u32 s31, s31, 0
	s_add_u32 s66, s24, s28
	s_addc_u32 s67, s25, s29
	s_add_u32 s68, s66, 0x180
	s_addc_u32 s69, s67, 0
	s_cmp_eq_u32 s60, s65
	s_cselect_b32 s67, s27, s31
	s_cselect_b32 s66, s26, s30
	s_cselect_b32 s31, s5, s69
	s_cselect_b32 s30, s4, s68
	s_add_u32 s76, s66, 0x80
	s_addc_u32 s77, s67, 0
	s_add_u32 s78, s30, 0x80
	s_addc_u32 s79, s31, 0
	s_add_i32 s68, s62, s42
	v_add_u32_e32 v131, 0, v128
	v_add_u32_e32 v182, 0, v127
.LBB6_22:
	s_mov_b32 m0, s68
	ds_read_b128 v[132:135], v131 offset:16384
	ds_read_b128 v[136:139], v131 offset:17408
	ds_read_b128 v[140:143], v131 offset:18432
	ds_read_b128 v[144:147], v131 offset:19456
	ds_read_b128 v[148:151], v182
	ds_read_b128 v[152:155], v182 offset:1024
	ds_read_b128 v[156:159], v182 offset:2048
	ds_read_b128 v[160:163], v182 offset:3072
	ds_read_b128 v[164:167], v182 offset:4096
	ds_read_b128 v[168:171], v182 offset:5120
	ds_read_b128 v[172:175], v182 offset:6144
	ds_read_b128 v[176:179], v182 offset:7168
	global_load_lds_dwordx4 v106, s[72:73]
	s_add_i32 m0, s68, 0x2000
	s_nop 0
	global_load_lds_dwordx4 v108, s[72:73]
	s_barrier
	s_setprio 1
	s_waitcnt lgkmcnt(7)
	v_mfma_f32_16x16x32_f16 v[40:43], v[132:135], v[148:151], v[40:43]
	v_mfma_f32_16x16x32_f16 v[44:47], v[140:143], v[148:151], v[44:47]
	s_waitcnt lgkmcnt(5)
	v_mfma_f32_16x16x32_f16 v[32:35], v[132:135], v[156:159], v[32:35]
	v_mfma_f32_16x16x32_f16 v[28:31], v[140:143], v[156:159], v[28:31]
	s_waitcnt lgkmcnt(3)
	v_mfma_f32_16x16x32_f16 v[20:23], v[132:135], v[164:167], v[20:23]
	v_mfma_f32_16x16x32_f16 v[16:19], v[140:143], v[164:167], v[16:19]
	s_waitcnt lgkmcnt(1)
	v_mfma_f32_16x16x32_f16 v[8:11], v[132:135], v[172:175], v[8:11]
	v_mfma_f32_16x16x32_f16 v[4:7], v[140:143], v[172:175], v[4:7]
	v_mfma_f32_16x16x32_f16 v[40:43], v[136:139], v[152:155], v[40:43]
	v_mfma_f32_16x16x32_f16 v[44:47], v[144:147], v[152:155], v[44:47]
	v_mfma_f32_16x16x32_f16 v[32:35], v[136:139], v[160:163], v[32:35]
	v_mfma_f32_16x16x32_f16 v[28:31], v[144:147], v[160:163], v[28:31]
	v_mfma_f32_16x16x32_f16 v[20:23], v[136:139], v[168:171], v[20:23]
	v_mfma_f32_16x16x32_f16 v[16:19], v[144:147], v[168:171], v[16:19]
	s_waitcnt lgkmcnt(0)
	v_mfma_f32_16x16x32_f16 v[8:11], v[136:139], v[176:179], v[8:11]
	v_mfma_f32_16x16x32_f16 v[4:7], v[144:147], v[176:179], v[4:7]
	s_setprio 0
	s_barrier
	s_add_i32 m0, s47, 0x18000
	ds_read_b128 v[132:135], v131 offset:20480
	ds_read_b128 v[136:139], v131 offset:21504
	global_load_lds_dwordx4 v110, s[74:75]
	s_add_i32 m0, s47, 0x1a000
	s_nop 0
	global_load_lds_dwordx4 v112, s[74:75]
	s_add_i32 m0, s47, 0x1c000
	s_nop 0
	global_load_lds_dwordx4 v114, s[74:75]
	s_cmp_lg_u32 s65, 0
	s_cbranch_scc1 .Lm2_norm_0
	s_mul_i32 s70, s58, 0xc0
	v_add_u32_e32 v234, s70, v129
	v_ashrrev_i32_e32 v235, 31, v234
	v_lshlrev_b64 v[234:235], 2, v[234:235]
	v_lshl_add_u64 v[234:235], s[18:19], 0, v[234:235]
	global_load_dwordx4 v[222:225], v[234:235], off
	global_load_dwordx4 v[226:229], v[234:235], off offset:64
	global_load_dwordx4 v[230:233], v[234:235], off offset:128
	global_load_dwordx2 v[198:199], v[190:191], off
	global_load_dwordx2 v[200:201], v[190:191], off offset:32
	global_load_dwordx2 v[202:203], v[190:191], off offset:64
	global_load_dwordx2 v[204:205], v[192:193], off
	s_waitcnt vmcnt(12)
	s_branch .Lm2_join_0

.Lm2_join_0:
	s_barrier
	s_setprio 1
	s_waitcnt lgkmcnt(1)
	v_mfma_f32_16x16x32_f16 v[36:39], v[132:135], v[148:151], v[36:39]
	v_mfma_f32_16x16x32_f16 v[24:27], v[132:135], v[156:159], v[24:27]
	v_mfma_f32_16x16x32_f16 v[12:15], v[132:135], v[164:167], v[12:15]
	v_mfma_f32_16x16x32_f16 v[0:3], v[132:135], v[172:175], v[0:3]
	s_waitcnt lgkmcnt(0)
	v_mfma_f32_16x16x32_f16 v[36:39], v[136:139], v[152:155], v[36:39]
	v_mfma_f32_16x16x32_f16 v[24:27], v[136:139], v[160:163], v[24:27]
	v_mfma_f32_16x16x32_f16 v[12:15], v[136:139], v[168:171], v[12:15]
	v_mfma_f32_16x16x32_f16 v[0:3], v[136:139], v[176:179], v[0:3]
	s_setprio 0
	s_barrier
	s_mov_b32 m0, s47
	ds_read_b128 v[132:135], v131 offset:57344
	ds_read_b128 v[136:139], v131 offset:58368
	ds_read_b128 v[140:143], v131 offset:59392
	ds_read_b128 v[144:147], v131 offset:60416
	ds_read_b128 v[148:151], v182 offset:40960
	ds_read_b128 v[152:155], v182 offset:41984
	ds_read_b128 v[156:159], v182 offset:43008
	ds_read_b128 v[160:163], v182 offset:44032
	ds_read_b128 v[164:167], v182 offset:45056
	ds_read_b128 v[168:171], v182 offset:46080
	ds_read_b128 v[172:175], v182 offset:47104
	ds_read_b128 v[176:179], v182 offset:48128
	global_load_lds_dwordx4 v48, s[66:67]
	s_mov_b32 m0, s48
	s_nop 0
	global_load_lds_dwordx4 v52, s[66:67]
	s_barrier
	s_setprio 1
	s_waitcnt lgkmcnt(7)
	v_mfma_f32_16x16x32_f16 v[40:43], v[132:135], v[148:151], v[40:43]
	v_mfma_f32_16x16x32_f16 v[44:47], v[140:143], v[148:151], v[44:47]
	s_waitcnt lgkmcnt(5)
	v_mfma_f32_16x16x32_f16 v[32:35], v[132:135], v[156:159], v[32:35]
	v_mfma_f32_16x16x32_f16 v[28:31], v[140:143], v[156:159], v[28:31]
	s_waitcnt lgkmcnt(3)
	v_mfma_f32_16x16x32_f16 v[20:23], v[132:135], v[164:167], v[20:23]
	v_mfma_f32_16x16x32_f16 v[16:19], v[140:143], v[164:167], v[16:19]
	s_waitcnt lgkmcnt(1)
	v_mfma_f32_16x16x32_f16 v[8:11], v[132:135], v[172:175], v[8:11]
	v_mfma_f32_16x16x32_f16 v[4:7], v[140:143], v[172:175], v[4:7]
	v_mfma_f32_16x16x32_f16 v[40:43], v[136:139], v[152:155], v[40:43]
	v_mfma_f32_16x16x32_f16 v[44:47], v[144:147], v[152:155], v[44:47]
	v_mfma_f32_16x16x32_f16 v[32:35], v[136:139], v[160:163], v[32:35]
	v_mfma_f32_16x16x32_f16 v[28:31], v[144:147], v[160:163], v[28:31]
	v_mfma_f32_16x16x32_f16 v[20:23], v[136:139], v[168:171], v[20:23]
	v_mfma_f32_16x16x32_f16 v[16:19], v[144:147], v[168:171], v[16:19]
	s_waitcnt lgkmcnt(0)
	v_mfma_f32_16x16x32_f16 v[8:11], v[136:139], v[176:179], v[8:11]
	v_mfma_f32_16x16x32_f16 v[4:7], v[144:147], v[176:179], v[4:7]
	s_setprio 0
	s_barrier
	s_mov_b32 m0, s49
	ds_read_b128 v[132:135], v131 offset:61440
	ds_read_b128 v[136:139], v131 offset:62464
	global_load_lds_dwordx4 v50, s[30:31]
	s_mov_b32 m0, s50
	s_nop 0
	global_load_lds_dwordx4 v54, s[30:31]
	s_mov_b32 m0, s51
	s_nop 0
	global_load_lds_dwordx4 v56, s[30:31]
	s_cmp_lg_u32 s65, 0
	s_cbranch_scc1 .Lm2_norm_1
	global_load_dwordx2 v[206:207], v[192:193], off offset:32
	global_load_dwordx2 v[208:209], v[192:193], off offset:64
	global_load_dwordx2 v[210:211], v[194:195], off
	global_load_dwordx2 v[212:213], v[194:195], off offset:32
	s_waitcnt vmcnt(16)
	s_branch .Lm2_join_1

.Lm2_join_1:
	s_barrier
	s_setprio 1
	s_waitcnt lgkmcnt(1)
	v_mfma_f32_16x16x32_f16 v[36:39], v[132:135], v[148:151], v[36:39]
	v_mfma_f32_16x16x32_f16 v[24:27], v[132:135], v[156:159], v[24:27]
	v_mfma_f32_16x16x32_f16 v[12:15], v[132:135], v[164:167], v[12:15]
	v_mfma_f32_16x16x32_f16 v[0:3], v[132:135], v[172:175], v[0:3]
	s_waitcnt lgkmcnt(0)
	v_mfma_f32_16x16x32_f16 v[36:39], v[136:139], v[152:155], v[36:39]
	v_mfma_f32_16x16x32_f16 v[24:27], v[136:139], v[160:163], v[24:27]
	v_mfma_f32_16x16x32_f16 v[12:15], v[136:139], v[168:171], v[12:15]
	v_mfma_f32_16x16x32_f16 v[0:3], v[136:139], v[176:179], v[0:3]
	s_setprio 0
	s_barrier
	s_mov_b32 m0, s54
	v_add_u32_e32 v131, s62, v127
	ds_read_b128 v[132:135], v130
	ds_read_b128 v[136:139], v130 offset:1024
	ds_read_b128 v[140:143], v130 offset:2048
	ds_read_b128 v[144:147], v130 offset:3072
	ds_read_b128 v[148:151], v131
	ds_read_b128 v[152:155], v131 offset:1024
	ds_read_b128 v[156:159], v131 offset:2048
	ds_read_b128 v[160:163], v131 offset:3072
	ds_read_b128 v[164:167], v131 offset:4096
	ds_read_b128 v[168:171], v131 offset:5120
	ds_read_b128 v[172:175], v131 offset:6144
	ds_read_b128 v[176:179], v131 offset:7168
	global_load_lds_dwordx4 v48, s[76:77]
	s_mov_b32 m0, s55
	s_nop 0
	global_load_lds_dwordx4 v52, s[76:77]
	s_barrier
	s_setprio 1
	s_waitcnt lgkmcnt(7)
	v_mfma_f32_16x16x32_f16 v[40:43], v[132:135], v[148:151], v[40:43]
	v_mfma_f32_16x16x32_f16 v[44:47], v[140:143], v[148:151], v[44:47]
	s_waitcnt lgkmcnt(5)
	v_mfma_f32_16x16x32_f16 v[32:35], v[132:135], v[156:159], v[32:35]
	v_mfma_f32_16x16x32_f16 v[28:31], v[140:143], v[156:159], v[28:31]
	s_waitcnt lgkmcnt(3)
	v_mfma_f32_16x16x32_f16 v[20:23], v[132:135], v[164:167], v[20:23]
	v_mfma_f32_16x16x32_f16 v[16:19], v[140:143], v[164:167], v[16:19]
	s_waitcnt lgkmcnt(1)
	v_mfma_f32_16x16x32_f16 v[8:11], v[132:135], v[172:175], v[8:11]
	v_mfma_f32_16x16x32_f16 v[4:7], v[140:143], v[172:175], v[4:7]
	v_mfma_f32_16x16x32_f16 v[40:43], v[136:139], v[152:155], v[40:43]
	v_mfma_f32_16x16x32_f16 v[44:47], v[144:147], v[152:155], v[44:47]
	v_mfma_f32_16x16x32_f16 v[32:35], v[136:139], v[160:163], v[32:35]
	v_mfma_f32_16x16x32_f16 v[28:31], v[144:147], v[160:163], v[28:31]
	v_mfma_f32_16x16x32_f16 v[20:23], v[136:139], v[168:171], v[20:23]
	v_mfma_f32_16x16x32_f16 v[16:19], v[144:147], v[168:171], v[16:19]
	s_waitcnt lgkmcnt(0)
	v_mfma_f32_16x16x32_f16 v[8:11], v[136:139], v[176:179], v[8:11]
	v_mfma_f32_16x16x32_f16 v[4:7], v[144:147], v[176:179], v[4:7]
	s_setprio 0
	s_barrier
	s_mov_b32 m0, s56
	ds_read_b128 v[132:135], v130 offset:4096
	ds_read_b128 v[136:139], v130 offset:5120
	global_load_lds_dwordx4 v50, s[78:79]
	s_add_i32 m0, s56, 0x2000
	s_nop 0
	global_load_lds_dwordx4 v54, s[78:79]
	s_add_i32 m0, s56, 0x4000
	s_nop 0
	global_load_lds_dwordx4 v56, s[78:79]
	s_cmp_lg_u32 s65, 0
	s_cbranch_scc1 .Lm2_norm_2
	global_load_dwordx2 v[214:215], v[194:195], off offset:64
	global_load_dwordx2 v[216:217], v[196:197], off
	global_load_dwordx2 v[218:219], v[196:197], off offset:32
	global_load_dwordx2 v[220:221], v[196:197], off offset:64
	s_waitcnt vmcnt(13)
	s_branch .Lm2_join_2

.Lm2_join_2:
	s_barrier
	s_setprio 1
	s_waitcnt lgkmcnt(1)
	v_mfma_f32_16x16x32_f16 v[36:39], v[132:135], v[148:151], v[36:39]
	v_mfma_f32_16x16x32_f16 v[24:27], v[132:135], v[156:159], v[24:27]
	v_mfma_f32_16x16x32_f16 v[12:15], v[132:135], v[164:167], v[12:15]
	v_mfma_f32_16x16x32_f16 v[0:3], v[132:135], v[172:175], v[0:3]
	s_waitcnt lgkmcnt(0)
	v_mfma_f32_16x16x32_f16 v[36:39], v[136:139], v[152:155], v[36:39]
	v_mfma_f32_16x16x32_f16 v[24:27], v[136:139], v[160:163], v[24:27]
	v_mfma_f32_16x16x32_f16 v[12:15], v[136:139], v[168:171], v[12:15]
	v_mfma_f32_16x16x32_f16 v[0:3], v[136:139], v[176:179], v[0:3]
	s_setprio 0
	s_add_i32 s65, s65, 3
	s_add_u32 s28, s28, 0x180
	s_addc_u32 s29, s29, 0
	s_cmp_ge_i32 s65, s59
	s_cbranch_scc1 .Lrot_exit_mlp2
	s_add_u32 s72, s22, s28
	s_addc_u32 s73, s23, s29
	s_add_u32 s74, s24, s28
	s_addc_u32 s75, s25, s29
	s_add_u32 s30, s22, s28
	s_addc_u32 s31, s23, s29
	s_add_u32 s30, s30, 0x180
	s_addc_u32 s31, s31, 0
	s_add_u32 s66, s24, s28
	s_addc_u32 s67, s25, s29
	s_add_u32 s68, s66, 0x180
	s_addc_u32 s69, s67, 0
	s_cmp_eq_u32 s60, s65
	s_cselect_b32 s67, s27, s31
	s_cselect_b32 s66, s26, s30
	s_cselect_b32 s31, s5, s69
	s_cselect_b32 s30, s4, s68
	s_add_u32 s76, s66, 0x80
	s_addc_u32 s77, s67, 0
	s_add_u32 s78, s30, 0x80
	s_addc_u32 s79, s31, 0
	s_add_i32 s68, s62, s42
	v_add_u32_e32 v131, 0, v128
	v_add_u32_e32 v182, 0, v127
	s_barrier
	s_branch .LBB6_22

	.amdhsa_kernel _Z9k_gemm192IN4g1927EpiResHEEvNS0_4GemmET_
		.amdhsa_group_segment_fixed_size 0
		.amdhsa_private_segment_fixed_size 0
		.amdhsa_kernarg_size 328
		.amdhsa_user_sgpr_count 2
		.amdhsa_user_sgpr_dispatch_ptr 0
		.amdhsa_user_sgpr_queue_ptr 0
		.amdhsa_user_sgpr_kernarg_segment_ptr 1
		.amdhsa_user_sgpr_dispatch_id 0
		.amdhsa_user_sgpr_kernarg_preload_length 0
		.amdhsa_user_sgpr_kernarg_preload_offset 0
		.amdhsa_user_sgpr_private_segment_size 0
		.amdhsa_uses_dynamic_stack 0
		.amdhsa_enable_private_segment 0
		.amdhsa_system_sgpr_workgroup_id_x 1
		.amdhsa_system_sgpr_workgroup_id_y 0
		.amdhsa_system_sgpr_workgroup_id_z 0
		.amdhsa_system_sgpr_workgroup_info 0
		.amdhsa_system_vgpr_workitem_id 0
		.amdhsa_next_free_vgpr 236
		.amdhsa_next_free_sgpr 80
		.amdhsa_accum_offset 236
		.amdhsa_reserve_vcc 1
		.amdhsa_float_round_mode_32 0
		.amdhsa_float_round_mode_16_64 0
		.amdhsa_float_denorm_mode_32 3
		.amdhsa_float_denorm_mode_16_64 3
		.amdhsa_dx10_clamp 1
		.amdhsa_ieee_mode 1
		.amdhsa_fp16_overflow 0
		.amdhsa_tg_split 0
		.amdhsa_exception_fp_ieee_invalid_op 0
		.amdhsa_exception_fp_denorm_src 0
		.amdhsa_exception_fp_ieee_div_zero 0
		.amdhsa_exception_fp_ieee_overflow 0
		.amdhsa_exception_fp_ieee_underflow 0
		.amdhsa_exception_fp_ieee_inexact 0
		.amdhsa_exception_int_div_zero 0
	.end_amdhsa_kernel
